# speedup vs baseline: 1.0181x; 1.0181x over previous
.LBB1_8:
	s_or_b64 exec, exec, s[4:5]
	s_waitcnt vmcnt(1)
	v_mov_b32_e32 v184, 1
	v_lshl_add_u32 v180, v176, 2, v172
	v_lshl_add_u32 v181, v177, 2, v172
	v_lshl_add_u32 v182, v178, 2, v172
	v_lshl_add_u32 v183, v179, 2, v172
	s_waitcnt lgkmcnt(0)
	ds_add_u32 v180, v184
	ds_add_u32 v181, v184
	ds_add_u32 v182, v184
	ds_add_u32 v183, v184
	s_waitcnt lgkmcnt(0)
	ds_read_b32 v151, v173
	s_waitcnt lgkmcnt(0)
	v_cvt_f32_i32_e32 v185, v151
	ds_write_b32 v173, v185 offset:256
	v_add_u32_e32 v10, v172, v2
	s_waitcnt vmcnt(1) lgkmcnt(0)
	s_barrier
	ds_read_b128 v[18:21], v10 offset:256
	ds_read_b128 v[22:25], v10 offset:288
	ds_read_b128 v[82:85], v10 offset:320
	ds_read_b128 v[86:89], v10 offset:352
	ds_read_b128 v[74:77], v10 offset:384
	ds_read_b128 v[78:81], v10 offset:416
	ds_read_b128 v[2:5], v213 offset:32768
	ds_read_b128 v[6:9], v213 offset:0
	ds_read_b128 v[66:69], v10 offset:448
	ds_read_b128 v[70:73], v10 offset:480
	ds_read_b128 v[10:13], v213 offset:1024
	s_waitcnt lgkmcnt(3)
	v_pk_mul_f32 v[26:27], v[8:9], v[20:21]
	v_pk_mul_f32 v[28:29], v[6:7], v[18:19]
	ds_read_b128 v[14:17], v213 offset:8192
	s_waitcnt lgkmcnt(1)
	v_pk_mul_f32 v[12:13], v[12:13], v[24:25]
	v_pk_mul_f32 v[10:11], v[10:11], v[22:23]
	v_pk_fma_f32 v[30:31], v[8:9], v[20:21], v[12:13]
	v_pk_fma_f32 v[32:33], v[6:7], v[18:19], v[10:11]
	v_cvt_pk_bf16_f32 v9, v12, v13
	v_cvt_pk_bf16_f32 v7, v26, v27
	v_cvt_pk_bf16_f32 v8, v10, v11
	v_cvt_pk_bf16_f32 v6, v28, v29
	ds_read_b128 v[10:13], v213 offset:33792
	s_nop 0
	v_mfma_f32_32x32x16_bf16 v[34:49], v[2:5], v[6:9], 0
	ds_read_b128 v[6:9], v213 offset:9216
	s_waitcnt lgkmcnt(2)
	v_mul_f32_e32 v26, v16, v20
	v_mul_f32_e32 v27, v17, v21
	v_pk_mul_f32 v[50:51], v[14:15], v[18:19]
	s_mov_b32 s4, 0x3727c5ac
	s_waitcnt lgkmcnt(0)
	v_pk_mul_f32 v[8:9], v[8:9], v[24:25]
	v_pk_mul_f32 v[28:29], v[6:7], v[22:23]
	v_pk_fma_f32 v[90:91], v[16:17], v[20:21], v[8:9]
	v_pk_fma_f32 v[92:93], v[14:15], v[18:19], v[28:29]
	ds_read_b128 v[14:17], v213 offset:2048
	v_cvt_pk_bf16_f32 v9, v8, v9
	v_cvt_pk_bf16_f32 v7, v26, v27
	v_cvt_pk_bf16_f32 v8, v28, v29
	ds_read_b128 v[26:29], v213 offset:3072
	v_cvt_pk_bf16_f32 v6, v50, v51
	s_waitcnt lgkmcnt(1)
	v_pk_mul_f32 v[94:95], v[14:15], v[82:83]
	s_mov_b32 s0, 0x3c800000
	v_mfma_f32_32x32x16_bf16 v[50:65], v[2:5], v[6:9], 0
	v_mul_f32_e32 v2, v16, v84
	v_mul_f32_e32 v3, v17, v85
	s_waitcnt lgkmcnt(0)
	v_mul_f32_e32 v4, v28, v88
	v_mul_f32_e32 v5, v29, v89
	v_pk_mul_f32 v[6:7], v[26:27], v[86:87]
	v_pk_fma_f32 v[8:9], v[16:17], v[84:85], v[4:5]
	v_cvt_pk_bf16_f32 v3, v2, v3
	v_pk_fma_f32 v[14:15], v[14:15], v[82:83], v[6:7]
	v_pk_add_f32 v[26:27], v[8:9], v[30:31]
	v_cvt_pk_bf16_f32 v5, v4, v5
	v_cvt_pk_bf16_f32 v4, v6, v7
	ds_read_b128 v[6:9], v213 offset:10240
	v_pk_add_f32 v[28:29], v[14:15], v[32:33]
	ds_read_b128 v[14:17], v213 offset:11264
	v_cvt_pk_bf16_f32 v2, v94, v95
	s_waitcnt lgkmcnt(1)
	v_pk_mul_f32 v[30:31], v[6:7], v[82:83]
	v_mov_b64_e32 v[152:153], s[4:5]
	v_mfma_f32_32x32x16_bf16 v[34:49], v[10:13], v[2:5], v[34:49]
	v_mul_f32_e32 v2, v8, v84
	v_mul_f32_e32 v3, v9, v85
	s_waitcnt lgkmcnt(0)
	v_mul_f32_e32 v4, v16, v88
	v_mul_f32_e32 v5, v17, v89
	v_pk_mul_f32 v[14:15], v[14:15], v[86:87]
	v_pk_fma_f32 v[8:9], v[8:9], v[84:85], v[4:5]
	v_pk_fma_f32 v[6:7], v[6:7], v[82:83], v[14:15]
	v_cvt_pk_bf16_f32 v5, v4, v5
	v_cvt_pk_bf16_f32 v3, v2, v3
	v_cvt_pk_bf16_f32 v4, v14, v15
	v_pk_add_f32 v[32:33], v[8:9], v[90:91]
	v_pk_add_f32 v[90:91], v[6:7], v[92:93]
	ds_read_b128 v[6:9], v213 offset:34816
	ds_read_b128 v[14:17], v213 offset:4096
	v_cvt_pk_bf16_f32 v2, v30, v31
	s_mov_b32 s13, 0
	s_mov_b64 s[6:7], 0
	v_mfma_f32_32x32x16_bf16 v[50:65], v[10:13], v[2:5], v[50:65]
	ds_read_b128 v[2:5], v213 offset:5120
	ds_read_b128 v[10:13], v213 offset:12288
	s_waitcnt lgkmcnt(2)
	v_pk_mul_f32 v[30:31], v[16:17], v[76:77]
	v_pk_mul_f32 v[92:93], v[14:15], v[74:75]
	s_waitcnt lgkmcnt(1)
	v_pk_mul_f32 v[4:5], v[4:5], v[80:81]
	v_pk_mul_f32 v[94:95], v[2:3], v[78:79]
	v_pk_fma_f32 v[2:3], v[16:17], v[76:77], v[4:5]
	v_cvt_pk_bf16_f32 v5, v4, v5
	v_pk_add_f32 v[96:97], v[2:3], v[26:27]
	v_cvt_pk_bf16_f32 v3, v30, v31
	v_cvt_pk_bf16_f32 v4, v94, v95
	v_cvt_pk_bf16_f32 v2, v92, v93
	v_pk_fma_f32 v[14:15], v[14:15], v[74:75], v[94:95]
	s_waitcnt lgkmcnt(0)
	v_pk_mul_f32 v[30:31], v[10:11], v[74:75]
	v_mfma_f32_32x32x16_bf16 v[34:49], v[6:9], v[2:5], v[34:49]
	ds_read_b128 v[2:5], v213 offset:13312
	v_add_f32_e32 v98, v14, v28
	v_add_f32_e32 v99, v15, v29
	ds_read_b128 v[14:17], v213 offset:35840
	v_pk_mul_f32 v[26:27], v[12:13], v[76:77]
	s_waitcnt lgkmcnt(1)
	v_pk_mul_f32 v[4:5], v[4:5], v[80:81]
	v_pk_mul_f32 v[28:29], v[2:3], v[78:79]
	v_pk_fma_f32 v[2:3], v[12:13], v[76:77], v[4:5]
	v_pk_fma_f32 v[10:11], v[10:11], v[74:75], v[28:29]
	v_pk_add_f32 v[32:33], v[2:3], v[32:33]
	v_pk_add_f32 v[92:93], v[10:11], v[90:91]
	ds_read_b128 v[10:13], v213 offset:6144
	v_cvt_pk_bf16_f32 v5, v4, v5
	v_cvt_pk_bf16_f32 v3, v26, v27
	v_cvt_pk_bf16_f32 v4, v28, v29
	ds_read_b128 v[26:29], v213 offset:7168
	v_cvt_pk_bf16_f32 v2, v30, v31
	s_waitcnt lgkmcnt(1)
	v_pk_mul_f32 v[30:31], v[10:11], v[66:67]
	v_mfma_f32_32x32x16_bf16 v[50:65], v[6:9], v[2:5], v[50:65]
	v_mul_f32_e32 v2, v12, v68
	v_mul_f32_e32 v3, v13, v69
	s_waitcnt lgkmcnt(0)
	v_mul_f32_e32 v4, v28, v72
	v_mul_f32_e32 v5, v29, v73
	v_pk_mul_f32 v[6:7], v[26:27], v[70:71]
	v_pk_fma_f32 v[8:9], v[12:13], v[68:69], v[4:5]
	v_cvt_pk_bf16_f32 v3, v2, v3
	v_pk_fma_f32 v[10:11], v[10:11], v[66:67], v[6:7]
	v_pk_add_f32 v[94:95], v[8:9], v[96:97]
	v_cvt_pk_bf16_f32 v5, v4, v5
	v_cvt_pk_bf16_f32 v4, v6, v7
	ds_read_b128 v[6:9], v213 offset:14336
	v_pk_add_f32 v[96:97], v[10:11], v[98:99]
	ds_read_b128 v[10:13], v213 offset:15360
	v_cvt_pk_bf16_f32 v2, v30, v31
	s_waitcnt lgkmcnt(1)
	v_pk_mul_f32 v[30:31], v[6:7], v[66:67]
	v_mfma_f32_32x32x16_bf16 v[34:49], v[14:17], v[2:5], v[34:49]
	s_waitcnt lgkmcnt(0)
	v_mul_f32_e32 v10, v10, v70
	v_mul_f32_e32 v11, v11, v71
	v_mul_f32_e32 v2, v8, v68
	v_mul_f32_e32 v3, v9, v69
	v_pk_mul_f32 v[4:5], v[12:13], v[72:73]
	v_pk_fma_f32 v[6:7], v[6:7], v[66:67], v[10:11]
	v_pk_fma_f32 v[8:9], v[8:9], v[68:69], v[4:5]
	v_pk_add_f32 v[92:93], v[6:7], v[92:93]
	v_cvt_pk_bf16_f32 v3, v2, v3
	v_pk_add_f32 v[90:91], v[8:9], v[32:33]
	v_cvt_pk_bf16_f32 v5, v4, v5
	v_cvt_pk_bf16_f32 v4, v10, v11
	ds_read_b128 v[26:29], v213 offset:36864
	ds_read_b128 v[6:9], v213 offset:16384
	v_cvt_pk_bf16_f32 v2, v30, v31
	ds_read_b128 v[98:101], v213 offset:25600
	ds_read_b128 v[102:105], v213 offset:37888
	v_mfma_f32_32x32x16_bf16 v[50:65], v[14:17], v[2:5], v[50:65]
	ds_read_b128 v[2:5], v213 offset:17408
	ds_read_b128 v[30:33], v213 offset:24576
	s_waitcnt lgkmcnt(4)
	v_pk_mul_f32 v[12:13], v[6:7], v[18:19]
	v_pk_mul_f32 v[10:11], v[8:9], v[20:21]
	s_waitcnt lgkmcnt(1)
	v_pk_mul_f32 v[14:15], v[2:3], v[22:23]
	v_pk_mul_f32 v[22:23], v[98:99], v[22:23]
	v_pk_fma_f32 v[112:113], v[6:7], v[18:19], v[14:15]
	s_waitcnt lgkmcnt(0)
	v_pk_mul_f32 v[114:115], v[30:31], v[18:19]
	v_pk_fma_f32 v[118:119], v[30:31], v[18:19], v[22:23]
	v_pk_mul_f32 v[4:5], v[4:5], v[24:25]
	v_pk_mul_f32 v[106:107], v[32:33], v[20:21]
	v_pk_mul_f32 v[24:25], v[100:101], v[24:25]
	ds_read_b128 v[98:101], v213 offset:18432
	v_cvt_pk_bf16_f32 v19, v106, v107
	ds_read_b128 v[106:109], v213 offset:19456
	v_pk_fma_f32 v[110:111], v[8:9], v[20:21], v[4:5]
	v_cvt_pk_bf16_f32 v5, v4, v5
	v_cvt_pk_bf16_f32 v3, v10, v11
	v_cvt_pk_bf16_f32 v4, v14, v15
	s_waitcnt lgkmcnt(0)
	v_pk_mul_f32 v[106:107], v[106:107], v[86:87]
	v_cvt_pk_bf16_f32 v2, v12, v13
	v_pk_mul_f32 v[120:121], v[98:99], v[82:83]
	v_pk_mul_f32 v[108:109], v[108:109], v[88:89]
	v_pk_fma_f32 v[98:99], v[98:99], v[82:83], v[106:107]
	v_mfma_f32_32x32x16_bf16 v[2:17], v[26:29], v[2:5], 0
	v_cvt_pk_bf16_f32 v18, v114, v115
	v_mul_f32_e32 v114, v100, v84
	v_mul_f32_e32 v115, v101, v85
	v_fma_f32 v100, v100, v84, v108
	v_fma_f32 v101, v101, v85, v109
	v_pk_add_f32 v[124:125], v[98:99], v[112:113]
	v_pk_add_f32 v[122:123], v[100:101], v[110:111]
	v_cvt_pk_bf16_f32 v101, v108, v109
	v_cvt_pk_bf16_f32 v100, v106, v107
	ds_read_b128 v[106:109], v213 offset:26624
	v_pk_fma_f32 v[116:117], v[32:33], v[20:21], v[24:25]
	v_cvt_pk_bf16_f32 v21, v24, v25
	v_cvt_pk_bf16_f32 v20, v22, v23
	ds_read_b128 v[110:113], v213 offset:27648
	v_cvt_pk_bf16_f32 v99, v114, v115
	v_mfma_f32_32x32x16_bf16 v[18:33], v[26:29], v[18:21], 0
	v_cvt_pk_bf16_f32 v98, v120, v121
	s_waitcnt lgkmcnt(1)
	v_mul_f32_e32 v114, v106, v82
	v_mul_f32_e32 v115, v107, v83
	s_waitcnt lgkmcnt(0)
	v_pk_mul_f32 v[86:87], v[110:111], v[86:87]
	v_pk_mul_f32 v[88:89], v[112:113], v[88:89]
	v_pk_fma_f32 v[82:83], v[106:107], v[82:83], v[86:87]
	v_mfma_f32_32x32x16_bf16 v[2:17], v[102:105], v[98:101], v[2:17]
	v_mul_f32_e32 v98, v108, v84
	v_mul_f32_e32 v99, v109, v85
	v_fma_f32 v84, v108, v84, v88
	v_fma_f32 v85, v109, v85, v89
	v_add_f32_e32 v108, v82, v118
	v_add_f32_e32 v109, v83, v119
	v_cvt_pk_bf16_f32 v83, v98, v99
	v_pk_add_f32 v[106:107], v[84:85], v[116:117]
	v_cvt_pk_bf16_f32 v85, v88, v89
	v_cvt_pk_bf16_f32 v84, v86, v87
	ds_read_b128 v[86:89], v213 offset:38912
	ds_read_b128 v[98:101], v213 offset:20480
	v_cvt_pk_bf16_f32 v82, v114, v115
	s_waitcnt lgkmcnt(0)
	v_pk_mul_f32 v[110:111], v[100:101], v[76:77]
	v_mfma_f32_32x32x16_bf16 v[18:33], v[102:105], v[82:85], v[18:33]
	ds_read_b128 v[82:85], v213 offset:21504
	ds_read_b128 v[102:105], v213 offset:28672
	v_mul_f32_e32 v112, v98, v74
	v_mul_f32_e32 v113, v99, v75
	s_waitcnt lgkmcnt(1)
	v_pk_mul_f32 v[84:85], v[84:85], v[80:81]
	v_pk_mul_f32 v[114:115], v[82:83], v[78:79]
	v_pk_fma_f32 v[82:83], v[100:101], v[76:77], v[84:85]
	v_cvt_pk_bf16_f32 v85, v84, v85
	v_pk_add_f32 v[116:117], v[82:83], v[122:123]
	v_cvt_pk_bf16_f32 v83, v110, v111
	v_cvt_pk_bf16_f32 v84, v114, v115
	v_cvt_pk_bf16_f32 v82, v112, v113
	v_pk_fma_f32 v[98:99], v[98:99], v[74:75], v[114:115]
	s_waitcnt lgkmcnt(0)
	v_pk_mul_f32 v[112:113], v[102:103], v[74:75]
	v_mfma_f32_32x32x16_bf16 v[2:17], v[86:89], v[82:85], v[2:17]
	ds_read_b128 v[82:85], v213 offset:29696
	v_add_f32_e32 v118, v98, v124
	v_add_f32_e32 v119, v99, v125
	v_mul_f32_e32 v110, v104, v76
	v_mul_f32_e32 v111, v105, v77
	ds_read_b128 v[98:101], v213 offset:39936
	s_waitcnt lgkmcnt(1)
	v_pk_mul_f32 v[78:79], v[82:83], v[78:79]
	v_pk_mul_f32 v[80:81], v[84:85], v[80:81]
	v_pk_fma_f32 v[74:75], v[102:103], v[74:75], v[78:79]
	v_pk_fma_f32 v[76:77], v[104:105], v[76:77], v[80:81]
	v_pk_add_f32 v[104:105], v[74:75], v[108:109]
	v_pk_add_f32 v[102:103], v[76:77], v[106:107]
	v_cvt_pk_bf16_f32 v77, v80, v81
	v_cvt_pk_bf16_f32 v76, v78, v79
	ds_read_b128 v[78:81], v213 offset:22528
	ds_read_b128 v[82:85], v213 offset:23552
	v_cvt_pk_bf16_f32 v75, v110, v111
	v_cvt_pk_bf16_f32 v74, v112, v113
	s_waitcnt lgkmcnt(0)
	v_pk_mul_f32 v[82:83], v[82:83], v[70:71]
	v_mfma_f32_32x32x16_bf16 v[18:33], v[86:89], v[74:77], v[18:33]
	v_mul_f32_e32 v74, v80, v68
	v_mul_f32_e32 v75, v81, v69
	v_mul_f32_e32 v76, v84, v72
	v_mul_f32_e32 v77, v85, v73
	v_mul_f32_e32 v86, v78, v66
	v_mul_f32_e32 v87, v79, v67
	v_pk_fma_f32 v[80:81], v[80:81], v[68:69], v[76:77]
	v_pk_fma_f32 v[78:79], v[78:79], v[66:67], v[82:83]
	v_cvt_pk_bf16_f32 v75, v74, v75
	v_pk_add_f32 v[88:89], v[80:81], v[116:117]
	v_pk_add_f32 v[106:107], v[78:79], v[118:119]
	ds_read_b128 v[78:81], v213 offset:30720
	v_cvt_pk_bf16_f32 v77, v76, v77
	v_cvt_pk_bf16_f32 v76, v82, v83
	ds_read_b128 v[82:85], v213 offset:31744
	v_cvt_pk_bf16_f32 v74, v86, v87
	s_waitcnt lgkmcnt(0)
	v_pk_mul_f32 v[72:73], v[84:85], v[72:73]
	v_mfma_f32_32x32x16_bf16 v[2:17], v[98:101], v[74:77], v[2:17]
	v_mul_f32_e32 v74, v80, v68
	v_mul_f32_e32 v75, v81, v69
	v_fma_f32 v68, v80, v68, v72
	v_fma_f32 v69, v81, v69, v73
	v_mul_f32_e32 v70, v82, v70
	v_mul_f32_e32 v71, v83, v71
	v_pk_add_f32 v[84:85], v[68:69], v[102:103]
	v_cvt_pk_bf16_f32 v69, v72, v73
	v_add_f32_e32 v72, v97, v96
	v_add_f32_e32 v73, v94, v95
	v_pk_mul_f32 v[76:77], v[78:79], v[66:67]
	v_pk_fma_f32 v[66:67], v[78:79], v[66:67], v[70:71]
	v_add_f32_e32 v72, v72, v73
	v_pk_add_f32 v[86:87], v[66:67], v[104:105]
	v_mov_b32_e32 v66, v72
	s_nop 1
	v_permlane32_swap_b32_e32 v72, v66
	v_add_f32_e32 v66, v72, v66
	v_cvt_pk_bf16_f32 v67, v74, v75
	v_rcp_f32_e32 v74, v66
	v_cvt_pk_bf16_f32 v68, v70, v71
	v_cvt_pk_bf16_f32 v66, v76, v77
	v_pk_mul_f32 v[70:71], v[46:47], v[74:75] op_sel_hi:[1,0]
	s_nop 0
	v_mfma_f32_32x32x16_bf16 v[18:33], v[98:101], v[66:69], v[18:33]
	v_mul_f32_e32 v66, v42, v74
	v_mul_f32_e32 v67, v43, v74
	v_add_f32_e32 v42, v93, v92
	v_add_f32_e32 v43, v90, v91
	v_pk_mul_f32 v[68:69], v[44:45], v[74:75] op_sel_hi:[1,0]
	v_add_f32_e32 v42, v42, v43
	v_mov_b32_e32 v43, v42
	s_nop 1
	v_permlane32_swap_b32_e32 v42, v43
	v_add_f32_e32 v42, v42, v43
	v_rcp_f32_e32 v42, v42
	v_add_f32_e32 v44, v107, v106
	v_add_f32_e32 v45, v88, v89
	v_pk_mul_f32 v[72:73], v[48:49], v[74:75] op_sel_hi:[1,0]
	v_add_f32_e32 v44, v44, v45
	v_pk_mul_f32 v[36:37], v[36:37], v[74:75] op_sel_hi:[1,0]
	v_pk_mul_f32 v[38:39], v[38:39], v[74:75] op_sel_hi:[1,0]
	v_pk_mul_f32 v[40:41], v[40:41], v[74:75] op_sel_hi:[1,0]
	v_pk_mul_f32 v[34:35], v[34:35], v[74:75] op_sel_hi:[1,0]
	v_pk_mul_f32 v[74:75], v[58:59], v[42:43] op_sel_hi:[1,0]
	v_pk_mul_f32 v[78:79], v[60:61], v[42:43] op_sel_hi:[1,0]
	v_pk_mul_f32 v[80:81], v[62:63], v[42:43] op_sel_hi:[1,0]
	v_pk_mul_f32 v[82:83], v[64:65], v[42:43] op_sel_hi:[1,0]
	v_pk_mul_f32 v[92:93], v[52:53], v[42:43] op_sel_hi:[1,0]
	v_mov_b32_e32 v43, v44
	s_nop 1
	v_permlane32_swap_b32_e32 v44, v43
	v_add_f32_e32 v43, v44, v43
	v_rcp_f32_e32 v76, v43
	v_pk_mul_f32 v[96:97], v[54:55], v[42:43] op_sel_hi:[1,0]
	v_pk_mul_f32 v[94:95], v[56:57], v[42:43] op_sel_hi:[1,0]
	v_pk_mul_f32 v[98:99], v[50:51], v[42:43] op_sel_hi:[1,0]
	v_pk_mul_f32 v[100:101], v[4:5], v[76:77] op_sel_hi:[1,0]
	v_pk_mov_b32 v[4:5], v[86:87], v[84:85] op_sel:[1,0]
	v_mov_b32_e32 v87, v85
	v_pk_add_f32 v[4:5], v[4:5], v[86:87]
	v_pk_mul_f32 v[102:103], v[6:7], v[76:77] op_sel_hi:[1,0]
	v_pk_add_f32 v[104:105], v[4:5], v[4:5] op_sel:[0,1] op_sel_hi:[1,0]
	v_cvt_pk_bf16_f32 v7, v40, v41
	ds_read_b128 v[84:87], v150 offset:52224
	ds_read_b128 v[50:53], v150 offset:35840
	ds_read_b128 v[54:57], v150 offset:36864
	ds_read_b128 v[58:61], v150 offset:37888
	ds_read_b128 v[62:65], v150 offset:38912
	v_cvt_pk_bf16_f32 v6, v38, v39
	v_cvt_pk_bf16_f32 v5, v36, v37
	v_cvt_pk_bf16_f32 v4, v34, v35
	ds_read_b128 v[88:91], v150 offset:53248
	ds_read_b128 v[34:37], v150 offset:39936
	ds_read_b128 v[38:41], v150 offset:40960
	ds_read_b128 v[42:45], v150 offset:41984
	ds_read_b128 v[46:49], v150 offset:43008
	v_cvt_pk_bf16_f32 v95, v94, v95
	v_cvt_pk_bf16_f32 v94, v96, v97
	v_cvt_pk_bf16_f32 v93, v92, v93
	v_cvt_pk_bf16_f32 v92, v98, v99
	s_waitcnt lgkmcnt(5)
	v_mfma_f32_32x32x16_bf16 v[50:65], v[84:87], v[4:7], v[50:65]
	v_mul_f32_e32 v10, v10, v76
	v_mul_f32_e32 v11, v11, v76
	v_mul_f32_e32 v12, v12, v76
	v_mul_f32_e32 v13, v13, v76
	v_mul_f32_e32 v8, v8, v76
	v_mul_f32_e32 v9, v9, v76
	v_mov_b32_e32 v77, v104
	s_nop 1
	v_permlane32_swap_b32_e32 v104, v77
	v_cvt_pk_bf16_f32 v73, v72, v73
	s_waitcnt lgkmcnt(0)
	v_mfma_f32_32x32x16_bf16 v[34:49], v[84:87], v[92:95], v[34:49]
	v_cvt_pk_bf16_f32 v72, v70, v71
	v_cvt_pk_bf16_f32 v70, v66, v67
	v_add_f32_e32 v66, v104, v77
	v_cvt_pk_bf16_f32 v71, v68, v69
	v_rcp_f32_e32 v104, v66
	v_cvt_pk_bf16_f32 v69, v82, v83
	v_cvt_pk_bf16_f32 v68, v80, v81
	v_cvt_pk_bf16_f32 v67, v78, v79
	v_cvt_pk_bf16_f32 v66, v74, v75
	ds_read_b128 v[78:81], v150 offset:54272
	v_mfma_f32_32x32x16_bf16 v[50:65], v[88:91], v[70:73], v[50:65]
	v_mul_f32_e32 v2, v2, v76
	v_mul_f32_e32 v3, v3, v76
	v_mul_f32_e32 v20, v20, v104
	v_mul_f32_e32 v21, v21, v104
	v_cvt_pk_bf16_f32 v85, v8, v9
	v_cvt_pk_bf16_f32 v82, v2, v3
	v_pk_mul_f32 v[2:3], v[22:23], v[104:105] op_sel_hi:[1,0]
	v_pk_mul_f32 v[8:9], v[24:25], v[104:105] op_sel_hi:[1,0]
	v_pk_mul_f32 v[18:19], v[18:19], v[104:105] op_sel_hi:[1,0]
	v_mfma_f32_32x32x16_bf16 v[34:49], v[88:91], v[66:69], v[34:49]
	v_cvt_pk_bf16_f32 v84, v102, v103
	v_cvt_pk_bf16_f32 v83, v100, v101
	ds_read_b128 v[86:89], v150 offset:55296
	v_cvt_pk_bf16_f32 v99, v8, v9
	v_cvt_pk_bf16_f32 v98, v2, v3
	v_cvt_pk_bf16_f32 v97, v20, v21
	v_cvt_pk_bf16_f32 v96, v18, v19
	s_waitcnt lgkmcnt(1)
	v_mfma_f32_32x32x16_bf16 v[50:65], v[78:81], v[82:85], v[50:65]
	v_mul_f32_e32 v2, v14, v76
	v_mul_f32_e32 v3, v15, v76
	v_mul_f32_e32 v8, v16, v76
	v_mul_f32_e32 v9, v17, v76
	v_mul_f32_e32 v14, v26, v104
	v_mul_f32_e32 v15, v27, v104
	v_cvt_pk_bf16_f32 v77, v8, v9
	v_cvt_pk_bf16_f32 v76, v2, v3
	v_cvt_pk_bf16_f32 v74, v10, v11
	v_pk_mul_f32 v[2:3], v[28:29], v[104:105] op_sel_hi:[1,0]
	v_mfma_f32_32x32x16_bf16 v[34:49], v[78:81], v[96:99], v[34:49]
	v_mul_f32_e32 v8, v30, v104
	v_mul_f32_e32 v9, v31, v104
	v_mul_f32_e32 v10, v32, v104
	v_mul_f32_e32 v11, v33, v104
	v_cvt_pk_bf16_f32 v75, v12, v13
	v_cvt_pk_bf16_f32 v81, v10, v11
	v_cvt_pk_bf16_f32 v80, v8, v9
	v_cvt_pk_bf16_f32 v79, v2, v3
	v_cvt_pk_bf16_f32 v78, v14, v15
	s_waitcnt lgkmcnt(0)
	v_mfma_f32_32x32x16_bf16 v[50:65], v[86:89], v[74:77], v[50:65]
	v_mfma_f32_32x32x16_bf16 v[34:49], v[86:89], v[78:81], v[34:49]
	ds_read_b128 v[86:89], v150 offset:56320
	ds_read_b128 v[18:21], v150 offset:44032
	ds_read_b128 v[22:25], v150 offset:45056
	ds_read_b128 v[26:29], v150 offset:46080
	ds_read_b128 v[30:33], v150 offset:47104
	ds_read_b128 v[100:103], v150 offset:57344
	s_waitcnt lgkmcnt(1)
	v_mfma_f32_32x32x16_bf16 v[18:33], v[86:89], v[4:7], v[18:33]
	ds_read_b128 v[2:5], v150 offset:48128
	ds_read_b128 v[6:9], v150 offset:49152
	ds_read_b128 v[10:13], v150 offset:50176
	ds_read_b128 v[14:17], v150 offset:51200
	s_waitcnt lgkmcnt(0)
	v_mfma_f32_32x32x16_bf16 v[2:17], v[86:89], v[92:95], v[2:17]
	v_mfma_f32_32x32x16_bf16 v[18:33], v[100:103], v[70:73], v[18:33]
	v_mfma_f32_32x32x16_bf16 v[2:17], v[100:103], v[66:69], v[2:17]
	ds_read_b128 v[66:69], v150 offset:58368
	ds_read_b128 v[70:73], v150 offset:59392
	s_waitcnt lgkmcnt(1)
	v_mfma_f32_32x32x16_bf16 v[18:33], v[66:69], v[82:85], v[18:33]
	v_mfma_f32_32x32x16_bf16 v[2:17], v[66:69], v[96:99], v[2:17]
	s_waitcnt lgkmcnt(0)
	v_mfma_f32_32x32x16_bf16 v[18:33], v[70:73], v[74:77], v[18:33]
	v_mfma_f32_32x32x16_bf16 v[2:17], v[70:73], v[78:81], v[2:17]
	s_nop 10
	v_mul_f32_e32 v66, v22, v22
	v_mul_f32_e32 v67, v23, v23
	v_mul_f32_e32 v68, v30, v30
	v_mul_f32_e32 v69, v31, v31
	v_mul_f32_e32 v70, v24, v24
	v_mul_f32_e32 v71, v25, v25
	v_pk_mul_f32 v[72:73], v[32:33], v[32:33]
	v_pk_mul_f32 v[74:75], v[20:21], v[20:21]
	v_pk_mul_f32 v[76:77], v[28:29], v[28:29]
	v_pk_mul_f32 v[78:79], v[26:27], v[26:27]
	v_pk_mul_f32 v[80:81], v[18:19], v[18:19]
	v_pk_fma_f32 v[78:79], v[58:59], v[58:59], v[78:79]
	v_pk_fma_f32 v[76:77], v[60:61], v[60:61], v[76:77]
	v_pk_fma_f32 v[74:75], v[52:53], v[52:53], v[74:75]
	v_pk_fma_f32 v[72:73], v[64:65], v[64:65], v[72:73]
	v_pk_fma_f32 v[70:71], v[56:57], v[56:57], v[70:71]
	v_pk_fma_f32 v[68:69], v[62:63], v[62:63], v[68:69]
	v_pk_fma_f32 v[66:67], v[54:55], v[54:55], v[66:67]
	v_pk_fma_f32 v[80:81], v[50:51], v[50:51], v[80:81]
	v_pk_add_f32 v[66:67], v[66:67], v[68:69]
	v_pk_add_f32 v[68:69], v[70:71], v[72:73]
	v_pk_add_f32 v[70:71], v[74:75], v[76:77]
	v_pk_add_f32 v[72:73], v[80:81], v[78:79]
	v_pk_add_f32 v[68:69], v[70:71], v[68:69]
	v_pk_add_f32 v[66:67], v[72:73], v[66:67]
	v_pk_mul_f32 v[72:73], v[14:15], v[14:15]
	v_pk_mov_b32 v[70:71], v[66:67], v[68:69] op_sel:[1,0]
	v_mov_b32_e32 v67, v69
	v_pk_add_f32 v[66:67], v[70:71], v[66:67]
	v_pk_mul_f32 v[70:71], v[6:7], v[6:7]
	v_pk_mul_f32 v[74:75], v[8:9], v[8:9]
	v_pk_mul_f32 v[76:77], v[16:17], v[16:17]
	v_pk_mul_f32 v[78:79], v[4:5], v[4:5]
	v_pk_mul_f32 v[80:81], v[12:13], v[12:13]
	v_pk_mul_f32 v[82:83], v[10:11], v[10:11]
	v_pk_mul_f32 v[84:85], v[2:3], v[2:3]
	v_pk_fma_f32 v[82:83], v[42:43], v[42:43], v[82:83]
	v_pk_fma_f32 v[80:81], v[44:45], v[44:45], v[80:81]
	v_pk_fma_f32 v[78:79], v[36:37], v[36:37], v[78:79]
	v_pk_fma_f32 v[76:77], v[48:49], v[48:49], v[76:77]
	v_pk_fma_f32 v[74:75], v[40:41], v[40:41], v[74:75]
	v_pk_fma_f32 v[72:73], v[46:47], v[46:47], v[72:73]
	v_pk_fma_f32 v[70:71], v[38:39], v[38:39], v[70:71]
	v_pk_fma_f32 v[84:85], v[34:35], v[34:35], v[84:85]
	v_pk_add_f32 v[70:71], v[70:71], v[72:73]
	v_pk_add_f32 v[72:73], v[74:75], v[76:77]
	v_pk_add_f32 v[74:75], v[78:79], v[80:81]
	v_pk_add_f32 v[76:77], v[84:85], v[82:83]
	v_pk_add_f32 v[72:73], v[74:75], v[72:73]
	v_pk_add_f32 v[70:71], v[76:77], v[70:71]
	v_pk_add_f32 v[66:67], v[66:67], v[66:67] op_sel:[0,1] op_sel_hi:[1,0]
	v_add_f32_e32 v70, v71, v70
	v_add_f32_e32 v71, v72, v73
	v_mov_b32_e32 v69, v66
	v_add_f32_e32 v70, v70, v71
	s_nop 0
	v_permlane32_swap_b32_e32 v66, v69
	v_mov_b32_e32 v68, v70
	s_nop 1
	v_permlane32_swap_b32_e32 v70, v68
	v_mov_b32_e32 v71, v66
	v_pk_add_f32 v[66:67], v[70:71], v[68:69]
	v_pk_fma_f32 v[66:67], v[66:67], s[0:1], v[152:153] op_sel_hi:[1,0,0]
	s_mov_b32 s1, 0x800000
	v_rsq_f32_e32 v68, v67
	s_nop 0
	v_pk_mul_f32 v[158:159], v[50:51], v[68:69] op_sel_hi:[1,0]
	v_pk_mul_f32 v[50:51], v[18:19], v[68:69] op_sel_hi:[1,0]
	v_pk_mul_f32 v[80:81], v[60:61], v[68:69] op_sel_hi:[1,0]
	v_pk_mul_f32 v[60:61], v[28:29], v[68:69] op_sel_hi:[1,0]
	v_pk_mul_f32 v[78:79], v[58:59], v[68:69] op_sel_hi:[1,0]
	v_pk_mul_f32 v[160:161], v[52:53], v[68:69] op_sel_hi:[1,0]
	v_pk_mul_f32 v[82:83], v[54:55], v[68:69] op_sel_hi:[1,0]
	v_rsq_f32_e32 v28, v66
	v_pk_mul_f32 v[168:169], v[56:57], v[68:69] op_sel_hi:[1,0]
	v_pk_mul_f32 v[58:59], v[26:27], v[68:69] op_sel_hi:[1,0]
	v_pk_mul_f32 v[52:53], v[20:21], v[68:69] op_sel_hi:[1,0]
	v_pk_mul_f32 v[54:55], v[22:23], v[68:69] op_sel_hi:[1,0]
	v_pk_mul_f32 v[56:57], v[24:25], v[68:69] op_sel_hi:[1,0]
	v_pk_mul_f32 v[18:19], v[42:43], v[28:29] op_sel_hi:[1,0]
	v_pk_mul_f32 v[20:21], v[44:45], v[28:29] op_sel_hi:[1,0]
	v_pk_mul_f32 v[22:23], v[46:47], v[28:29] op_sel_hi:[1,0]
	v_pk_mul_f32 v[26:27], v[48:49], v[28:29] op_sel_hi:[1,0]
	v_pk_mul_f32 v[162:163], v[34:35], v[28:29] op_sel_hi:[1,0]
	v_pk_mul_f32 v[164:165], v[36:37], v[28:29] op_sel_hi:[1,0]
	v_pk_mul_f32 v[166:167], v[38:39], v[28:29] op_sel_hi:[1,0]
	v_pk_mul_f32 v[24:25], v[40:41], v[28:29] op_sel_hi:[1,0]
	v_pk_mul_f32 v[104:105], v[2:3], v[28:29] op_sel_hi:[1,0]
	v_pk_mul_f32 v[112:113], v[4:5], v[28:29] op_sel_hi:[1,0]
	ds_read_b128 v[2:5], v150 offset:60416
	ds_read_b128 v[34:37], v174 offset:32768
	ds_read_b128 v[38:41], v174 offset:32800
	ds_read_b128 v[42:45], v174 offset:32832
	ds_read_b128 v[46:49], v174 offset:32864
	v_cvt_pk_bf16_f32 v129, v168, v169
	v_cvt_pk_bf16_f32 v128, v82, v83
	v_cvt_pk_bf16_f32 v127, v160, v161
	v_cvt_pk_bf16_f32 v126, v158, v159
	v_cvt_pk_bf16_f32 v137, v24, v25
	v_cvt_pk_bf16_f32 v136, v166, v167
	v_cvt_pk_bf16_f32 v135, v164, v165
	s_waitcnt lgkmcnt(0)
	v_mfma_f32_32x32x16_bf16 v[86:101], v[2:5], v[126:129], v[34:49]
	v_cvt_pk_bf16_f32 v134, v162, v163
	v_mul_f32_e32 v84, v62, v68
	v_mul_f32_e32 v85, v63, v68
	v_mul_f32_e32 v170, v64, v68
	v_mul_f32_e32 v171, v65, v68
	v_pk_mul_f32 v[62:63], v[30:31], v[68:69] op_sel_hi:[1,0]
	v_pk_mul_f32 v[64:65], v[32:33], v[68:69] op_sel_hi:[1,0]
	v_pk_mul_f32 v[116:117], v[6:7], v[28:29] op_sel_hi:[1,0]
	v_pk_mul_f32 v[154:155], v[8:9], v[28:29] op_sel_hi:[1,0]
	v_mfma_f32_32x32x16_bf16 v[34:49], v[2:5], v[134:137], v[34:49]
	ds_read_b128 v[6:9], v150 offset:61440
	ds_read_b128 v[66:69], v174 offset:32896
	ds_read_b128 v[106:109], v150 offset:64512
	v_cvt_pk_bf16_f32 v125, v170, v171
	v_cvt_pk_bf16_f32 v124, v84, v85
	v_cvt_pk_bf16_f32 v123, v80, v81
	v_cvt_pk_bf16_f32 v122, v78, v79
	v_cvt_pk_bf16_f32 v149, v26, v27
	v_cvt_pk_bf16_f32 v148, v22, v23
	v_cvt_pk_bf16_f32 v147, v20, v21
	v_cvt_pk_bf16_f32 v146, v18, v19
	s_waitcnt lgkmcnt(2)
	v_mfma_f32_32x32x16_bf16 v[86:101], v[6:9], v[122:125], v[86:101]
	v_mul_f32_e32 v102, v10, v28
	v_mul_f32_e32 v103, v11, v28
	v_mul_f32_e32 v110, v12, v28
	v_mul_f32_e32 v111, v13, v28
	v_mul_f32_e32 v114, v14, v28
	v_mul_f32_e32 v115, v15, v28
	v_pk_mul_f32 v[156:157], v[16:17], v[28:29] op_sel_hi:[1,0]
	ds_read_b128 v[176:179], v174 offset:33536
	ds_read_b128 v[180:183], v174 offset:33568
	ds_read_b128 v[184:187], v174 offset:33600
	ds_read_b128 v[28:31], v174 offset:33632
	ds_read_b128 v[188:191], v174 offset:33792
	ds_read_b128 v[192:195], v174 offset:33824
	ds_read_b128 v[196:199], v174 offset:33856
	ds_read_b128 v[200:203], v174 offset:33888
	ds_read_b128 v[204:207], v150 offset:62464
	v_cvt_pk_bf16_f32 v133, v56, v57
	v_mfma_f32_32x32x16_bf16 v[34:49], v[6:9], v[146:149], v[34:49]
	v_cvt_pk_bf16_f32 v132, v54, v55
	v_cvt_pk_bf16_f32 v131, v52, v53
	v_cvt_pk_bf16_f32 v130, v50, v51
	ds_read_b128 v[70:73], v174 offset:33664
	ds_read_b128 v[74:77], v174 offset:33920
	ds_read_b128 v[208:211], v150 offset:63488
	v_cvt_pk_bf16_f32 v145, v154, v155
	v_cvt_pk_bf16_f32 v144, v116, v117
	v_cvt_pk_bf16_f32 v143, v112, v113
	v_cvt_pk_bf16_f32 v142, v104, v105
	s_waitcnt lgkmcnt(3)
	v_mfma_f32_32x32x16_bf16 v[86:101], v[204:207], v[130:133], v[86:101]
	v_cvt_pk_bf16_f32 v121, v64, v65
	v_cvt_pk_bf16_f32 v120, v62, v63
	v_cvt_pk_bf16_f32 v119, v60, v61
	v_cvt_pk_bf16_f32 v118, v58, v59
	v_cvt_pk_bf16_f32 v141, v156, v157
	v_cvt_pk_bf16_f32 v140, v114, v115
	v_cvt_pk_bf16_f32 v139, v110, v111
	v_mfma_f32_32x32x16_bf16 v[34:49], v[204:207], v[142:145], v[34:49]
	v_cvt_pk_bf16_f32 v138, v102, v103
	v_fma_f32 v16, v30, v170, v202
	v_fma_f32 v17, v31, v171, v203
	v_fma_f32 v14, v28, v84, v200
	v_fma_f32 v15, v29, v85, v201
	v_pk_fma_f32 v[12:13], v[186:187], v[80:81], v[198:199]
	v_pk_fma_f32 v[10:11], v[184:185], v[78:79], v[196:197]
	v_pk_fma_f32 v[8:9], v[182:183], v[168:169], v[194:195]
	s_waitcnt lgkmcnt(0)
	v_mfma_f32_32x32x16_bf16 v[86:101], v[208:211], v[118:121], v[86:101]
	v_fma_f32 v6, v180, v82, v192
	v_fma_f32 v7, v181, v83, v193
	ds_read_b128 v[78:81], v174 offset:33760
	ds_read_b128 v[82:85], v174 offset:33248
	v_fma_f32 v4, v178, v160, v190
	v_fma_f32 v5, v179, v161, v191
	v_pk_fma_f32 v[2:3], v[176:177], v[158:159], v[188:189]
	v_pk_fma_f32 v[32:33], v[30:31], v[26:27], v[202:203]
	v_pk_fma_f32 v[30:31], v[28:29], v[22:23], v[200:201]
	v_pk_fma_f32 v[28:29], v[186:187], v[20:21], v[198:199]
	v_pk_fma_f32 v[26:27], v[184:185], v[18:19], v[196:197]
	v_pk_fma_f32 v[24:25], v[182:183], v[24:25], v[194:195]
	v_pk_fma_f32 v[22:23], v[180:181], v[166:167], v[192:193]
	v_pk_fma_f32 v[20:21], v[178:179], v[164:165], v[190:191]
	v_pk_fma_f32 v[18:19], v[176:177], v[162:163], v[188:189]
	ds_read_b128 v[158:161], v174 offset:33696
	ds_read_b128 v[162:165], v174 offset:33728
	ds_read_b128 v[166:169], v174 offset:33952
	ds_read_b128 v[176:179], v174 offset:33984
	ds_read_b128 v[180:183], v174 offset:34016
	ds_read_b128 v[184:187], v212 offset:11264
	v_mfma_f32_32x32x16_bf16 v[34:49], v[208:211], v[138:141], v[34:49]
	v_cvt_pk_bf16_f32 v86, v86, v87
	v_cvt_pk_bf16_f32 v87, v88, v89
	v_cvt_pk_bf16_f32 v88, v90, v91
	v_cvt_pk_bf16_f32 v89, v92, v93
	ds_read_b128 v[90:93], v212 offset:12288
	v_pk_max_i16 v86, v86, 0
	v_pk_max_i16 v87, v87, 0
	v_pk_max_i16 v88, v88, 0
	v_pk_max_i16 v89, v89, 0
	s_nop 1
	s_nop 0
	v_cvt_pk_bf16_f32 v188, v34, v35
	v_cvt_pk_bf16_f32 v189, v36, v37
	v_cvt_pk_bf16_f32 v190, v38, v39
	v_cvt_pk_bf16_f32 v191, v40, v41
	s_waitcnt lgkmcnt(1)
	v_mfma_f32_32x32x16_bf16 v[2:17], v[184:187], v[86:89], v[2:17]
	v_pk_max_i16 v188, v188, 0
	v_pk_max_i16 v189, v189, 0
	v_pk_max_i16 v190, v190, 0
	v_pk_max_i16 v191, v191, 0
	v_cvt_pk_bf16_f32 v94, v94, v95
	v_cvt_pk_bf16_f32 v95, v96, v97
	v_cvt_pk_bf16_f32 v96, v98, v99
	v_cvt_pk_bf16_f32 v97, v100, v101
	v_cvt_pk_bf16_f32 v98, v42, v43
	v_cvt_pk_bf16_f32 v99, v44, v45
	v_mfma_f32_32x32x16_bf16 v[18:33], v[184:187], v[188:191], v[18:33]
	ds_read_b128 v[184:187], v212 offset:19456
	v_cvt_pk_bf16_f32 v100, v46, v47
	v_cvt_pk_bf16_f32 v101, v48, v49
	v_fma_f32 v64, v80, v64, v182
	v_fma_f32 v65, v81, v65, v183
	v_pk_fma_f32 v[62:63], v[78:79], v[62:63], v[180:181]
	v_pk_fma_f32 v[60:61], v[164:165], v[60:61], v[178:179]
	v_pk_fma_f32 v[58:59], v[162:163], v[58:59], v[176:177]
	v_pk_max_i16 v94, v94, 0
	v_pk_max_i16 v95, v95, 0
	v_pk_max_i16 v96, v96, 0
	v_pk_max_i16 v97, v97, 0
	v_pk_max_i16 v98, v98, 0
	v_pk_max_i16 v99, v99, 0
	v_pk_max_i16 v100, v100, 0
	v_pk_max_i16 v101, v101, 0
	v_pk_fma_f32 v[56:57], v[160:161], v[56:57], v[168:169]
	s_waitcnt lgkmcnt(1)
	v_mfma_f32_32x32x16_bf16 v[2:17], v[90:93], v[94:97], v[2:17]
	v_fma_f32 v54, v158, v54, v166
	v_fma_f32 v55, v159, v55, v167
	v_fma_f32 v52, v72, v52, v76
	v_fma_f32 v53, v73, v53, v77
	v_fma_f32 v50, v70, v50, v74
	v_fma_f32 v51, v71, v51, v75
	v_pk_fma_f32 v[48:49], v[80:81], v[156:157], v[182:183]
	v_pk_fma_f32 v[46:47], v[78:79], v[114:115], v[180:181]
	v_pk_fma_f32 v[44:45], v[164:165], v[110:111], v[178:179]
	v_pk_fma_f32 v[42:43], v[162:163], v[102:103], v[176:177]
	v_mfma_f32_32x32x16_bf16 v[18:33], v[90:93], v[98:101], v[18:33]
	ds_read_b128 v[90:93], v212 offset:20480
	v_fma_f32 v40, v160, v154, v168
	v_fma_f32 v41, v161, v155, v169
	v_fma_f32 v38, v158, v116, v166
	v_fma_f32 v39, v159, v117, v167
	v_pk_fma_f32 v[36:37], v[72:73], v[112:113], v[76:77]
	v_pk_fma_f32 v[34:35], v[70:71], v[104:105], v[74:75]
	s_waitcnt lgkmcnt(1)
	v_mfma_f32_32x32x16_bf16 v[50:65], v[184:187], v[86:89], v[50:65]
	ds_read_b128 v[70:73], v174 offset:32928
	ds_read_b128 v[74:77], v174 offset:32960
	ds_read_b128 v[78:81], v174 offset:32992
	ds_read_b128 v[86:89], v174 offset:33024
	ds_read_b128 v[110:113], v212 offset:1024
	v_mfma_f32_32x32x16_bf16 v[34:49], v[184:187], v[188:191], v[34:49]
	s_waitcnt lgkmcnt(5)
	v_mfma_f32_32x32x16_bf16 v[50:65], v[90:93], v[94:97], v[50:65]
	v_mfma_f32_32x32x16_bf16 v[34:49], v[90:93], v[98:101], v[34:49]
	s_waitcnt lgkmcnt(2)
	v_mfma_f32_32x32x16_bf16 v[90:105], v[106:109], v[126:129], v[66:81]
	v_mfma_f32_32x32x16_bf16 v[66:81], v[106:109], v[134:137], v[66:81]
	ds_read_b128 v[106:109], v212 offset:0
	s_waitcnt lgkmcnt(0)
	v_mfma_f32_32x32x16_bf16 v[90:105], v[106:109], v[122:125], v[90:105]
	v_mfma_f32_32x32x16_bf16 v[66:81], v[106:109], v[146:149], v[66:81]
	ds_read_b128 v[106:109], v212 offset:2048
	v_mfma_f32_32x32x16_bf16 v[90:105], v[110:113], v[130:133], v[90:105]
	v_mfma_f32_32x32x16_bf16 v[66:81], v[110:113], v[142:145], v[66:81]
	ds_read_b128 v[110:113], v212 offset:13312
	s_waitcnt lgkmcnt(1)
	v_mfma_f32_32x32x16_bf16 v[90:105], v[106:109], v[118:121], v[90:105]
	v_mfma_f32_32x32x16_bf16 v[66:81], v[106:109], v[138:141], v[66:81]
	s_nop 10
	v_cvt_pk_bf16_f32 v90, v90, v91
	v_cvt_pk_bf16_f32 v91, v92, v93
	v_cvt_pk_bf16_f32 v92, v94, v95
	v_cvt_pk_bf16_f32 v94, v98, v99
	v_cvt_pk_bf16_f32 v95, v100, v101
	ds_read_b128 v[98:101], v212 offset:21504
	v_cvt_pk_bf16_f32 v66, v66, v67
	v_cvt_pk_bf16_f32 v67, v68, v69
	v_cvt_pk_bf16_f32 v68, v70, v71
	v_cvt_pk_bf16_f32 v93, v96, v97
	v_cvt_pk_bf16_f32 v69, v72, v73
	ds_read_b128 v[70:73], v212 offset:14336
	v_pk_max_i16 v90, v90, 0
	v_pk_max_i16 v91, v91, 0
	v_pk_max_i16 v92, v92, 0
	v_pk_max_i16 v93, v93, 0
	v_pk_max_i16 v66, v66, 0
	v_pk_max_i16 v67, v67, 0
	v_pk_max_i16 v68, v68, 0
	v_pk_max_i16 v69, v69, 0
	v_cvt_pk_bf16_f32 v96, v102, v103
	s_waitcnt lgkmcnt(2)
	v_mfma_f32_32x32x16_bf16 v[2:17], v[110:113], v[90:93], v[2:17]
	v_cvt_pk_bf16_f32 v97, v104, v105
	v_cvt_pk_bf16_f32 v74, v74, v75
	v_cvt_pk_bf16_f32 v75, v76, v77
	v_cvt_pk_bf16_f32 v76, v78, v79
	v_cvt_pk_bf16_f32 v77, v80, v81
	v_pk_max_i16 v94, v94, 0
	v_pk_max_i16 v95, v95, 0
	v_pk_max_i16 v96, v96, 0
	v_pk_max_i16 v97, v97, 0
	v_pk_max_i16 v74, v74, 0
	v_pk_max_i16 v75, v75, 0
	v_pk_max_i16 v76, v76, 0
	v_pk_max_i16 v77, v77, 0
	v_mfma_f32_32x32x16_bf16 v[18:33], v[110:113], v[66:69], v[18:33]
	s_waitcnt lgkmcnt(1)
	v_mfma_f32_32x32x16_bf16 v[34:49], v[98:101], v[66:69], v[34:49]
	ds_read_b128 v[66:69], v212 offset:22528
	v_mfma_f32_32x32x16_bf16 v[50:65], v[98:101], v[90:93], v[50:65]
	s_waitcnt lgkmcnt(1)
	v_mfma_f32_32x32x16_bf16 v[2:17], v[70:73], v[94:97], v[2:17]
	v_mfma_f32_32x32x16_bf16 v[18:33], v[70:73], v[74:77], v[18:33]
	ds_read_b128 v[78:81], v212 offset:3072
	s_waitcnt lgkmcnt(1)
	v_mfma_f32_32x32x16_bf16 v[50:65], v[66:69], v[94:97], v[50:65]
	ds_read_b128 v[90:93], v174 offset:33056
	ds_read_b128 v[94:97], v174 offset:33088
	ds_read_b128 v[98:101], v174 offset:33120
	ds_read_b128 v[70:73], v174 offset:33152
	v_mfma_f32_32x32x16_bf16 v[34:49], v[66:69], v[74:77], v[34:49]
	ds_read_b128 v[66:69], v212 offset:4096
	ds_read_b128 v[74:77], v212 offset:5120
	s_waitcnt lgkmcnt(3)
	v_mfma_f32_32x32x16_bf16 v[102:117], v[78:81], v[126:129], v[86:101]
	v_mfma_f32_32x32x16_bf16 v[86:101], v[78:81], v[134:137], v[86:101]
	s_waitcnt lgkmcnt(1)
	v_mfma_f32_32x32x16_bf16 v[86:101], v[66:69], v[146:149], v[86:101]
	v_mfma_f32_32x32x16_bf16 v[102:117], v[66:69], v[122:125], v[102:117]
	ds_read_b128 v[66:69], v212 offset:6144
	s_waitcnt lgkmcnt(1)
	v_mfma_f32_32x32x16_bf16 v[86:101], v[74:77], v[142:145], v[86:101]
	v_mfma_f32_32x32x16_bf16 v[102:117], v[74:77], v[130:133], v[102:117]
	ds_read_b128 v[74:77], v212 offset:15360
	s_waitcnt lgkmcnt(1)
	v_mfma_f32_32x32x16_bf16 v[86:101], v[66:69], v[138:141], v[86:101]
	v_mfma_f32_32x32x16_bf16 v[102:117], v[66:69], v[118:121], v[102:117]
	s_nop 10
	v_cvt_pk_bf16_f32 v78, v86, v87
	v_cvt_pk_bf16_f32 v80, v90, v91
	v_cvt_pk_bf16_f32 v79, v88, v89
	v_cvt_pk_bf16_f32 v81, v92, v93
	ds_read_b128 v[86:89], v212 offset:16384
	ds_read_b128 v[90:93], v212 offset:23552
	v_cvt_pk_bf16_f32 v66, v102, v103
	v_cvt_pk_bf16_f32 v67, v104, v105
	v_cvt_pk_bf16_f32 v68, v106, v107
	v_cvt_pk_bf16_f32 v69, v108, v109
	v_pk_max_i16 v66, v66, 0
	v_pk_max_i16 v67, v67, 0
	v_pk_max_i16 v68, v68, 0
	v_pk_max_i16 v69, v69, 0
	v_pk_max_i16 v78, v78, 0
	v_pk_max_i16 v79, v79, 0
	v_pk_max_i16 v80, v80, 0
	v_pk_max_i16 v81, v81, 0
	v_cvt_pk_bf16_f32 v94, v94, v95
	s_waitcnt lgkmcnt(2)
	v_mfma_f32_32x32x16_bf16 v[18:33], v[74:77], v[78:81], v[18:33]
	v_cvt_pk_bf16_f32 v95, v96, v97
	v_cvt_pk_bf16_f32 v96, v98, v99
	v_cvt_pk_bf16_f32 v97, v100, v101
	v_pk_max_i16 v94, v94, 0
	v_pk_max_i16 v95, v95, 0
	v_pk_max_i16 v96, v96, 0
	v_pk_max_i16 v97, v97, 0
	v_mfma_f32_32x32x16_bf16 v[2:17], v[74:77], v[66:69], v[2:17]
	v_cvt_pk_bf16_f32 v74, v110, v111
	v_cvt_pk_bf16_f32 v75, v112, v113
	v_cvt_pk_bf16_f32 v76, v114, v115
	v_cvt_pk_bf16_f32 v77, v116, v117
	v_pk_max_i16 v74, v74, 0
	v_pk_max_i16 v75, v75, 0
	v_pk_max_i16 v76, v76, 0
	v_pk_max_i16 v77, v77, 0
	s_waitcnt lgkmcnt(0)
	v_mfma_f32_32x32x16_bf16 v[50:65], v[90:93], v[66:69], v[50:65]
	ds_read_b128 v[66:69], v212 offset:24576
	v_mfma_f32_32x32x16_bf16 v[34:49], v[90:93], v[78:81], v[34:49]
	ds_read_b128 v[102:105], v212 offset:7168
	v_mfma_f32_32x32x16_bf16 v[2:17], v[86:89], v[74:77], v[2:17]
	s_waitcnt lgkmcnt(1)
	v_mfma_f32_32x32x16_bf16 v[50:65], v[66:69], v[74:77], v[50:65]
	ds_read_b128 v[74:77], v174 offset:33184
	ds_read_b128 v[78:81], v174 offset:33216
	v_mfma_f32_32x32x16_bf16 v[34:49], v[66:69], v[94:97], v[34:49]
	ds_read_b128 v[66:69], v212 offset:8192
	v_mfma_f32_32x32x16_bf16 v[18:33], v[86:89], v[94:97], v[18:33]
	s_waitcnt lgkmcnt(1)
	v_mfma_f32_32x32x16_bf16 v[86:101], v[102:105], v[126:129], v[70:85]
	v_mfma_f32_32x32x16_bf16 v[70:85], v[102:105], v[134:137], v[70:85]
	ds_read_b128 v[102:105], v212 offset:9216
	v_lshlrev_b32_e32 v135, 2, v1
	v_add_u32_e32 v134, v172, v174
	s_waitcnt lgkmcnt(1)
	v_mfma_f32_32x32x16_bf16 v[86:101], v[66:69], v[122:125], v[86:101]
	v_mfma_f32_32x32x16_bf16 v[70:85], v[66:69], v[146:149], v[70:85]
	ds_read_b128 v[66:69], v212 offset:10240
	s_waitcnt lgkmcnt(1)
	v_mfma_f32_32x32x16_bf16 v[86:101], v[102:105], v[130:133], v[86:101]
	v_mfma_f32_32x32x16_bf16 v[70:85], v[102:105], v[142:145], v[70:85]
	ds_read_b128 v[102:105], v212 offset:17408
	s_waitcnt lgkmcnt(1)
	v_mfma_f32_32x32x16_bf16 v[86:101], v[66:69], v[118:121], v[86:101]
	v_mfma_f32_32x32x16_bf16 v[70:85], v[66:69], v[138:141], v[70:85]
	s_nop 10
	v_cvt_pk_bf16_f32 v68, v90, v91
	v_cvt_pk_bf16_f32 v69, v92, v93
	ds_read_b128 v[90:93], v212 offset:25600
	v_cvt_pk_bf16_f32 v66, v86, v87
	v_cvt_pk_bf16_f32 v67, v88, v89
	v_pk_max_i16 v66, v66, 0
	v_pk_max_i16 v67, v67, 0
	v_pk_max_i16 v68, v68, 0
	v_pk_max_i16 v69, v69, 0
	v_cvt_pk_bf16_f32 v70, v70, v71
	v_cvt_pk_bf16_f32 v71, v72, v73
	s_waitcnt lgkmcnt(1)
	v_mfma_f32_32x32x16_bf16 v[2:17], v[102:105], v[66:69], v[2:17]
	v_cvt_pk_bf16_f32 v72, v74, v75
	v_cvt_pk_bf16_f32 v73, v76, v77
	ds_read_b128 v[74:77], v212 offset:18432
	v_cvt_pk_bf16_f32 v86, v94, v95
	v_cvt_pk_bf16_f32 v87, v96, v97
	v_cvt_pk_bf16_f32 v88, v98, v99
	s_waitcnt lgkmcnt(1)
	v_mfma_f32_32x32x16_bf16 v[50:65], v[90:93], v[66:69], v[50:65]
	ds_read_b128 v[66:69], v212 offset:26624
	v_cvt_pk_bf16_f32 v89, v100, v101
	v_pk_max_i16 v86, v86, 0
	v_pk_max_i16 v87, v87, 0
	v_pk_max_i16 v88, v88, 0
	v_pk_max_i16 v89, v89, 0
	v_pk_max_i16 v70, v70, 0
	v_pk_max_i16 v71, v71, 0
	v_pk_max_i16 v72, v72, 0
	v_pk_max_i16 v73, v73, 0
	v_cvt_pk_bf16_f32 v78, v78, v79
	v_cvt_pk_bf16_f32 v79, v80, v81
	s_waitcnt lgkmcnt(1)
	v_mfma_f32_32x32x16_bf16 v[2:17], v[74:77], v[86:89], v[2:17]
	v_cvt_pk_bf16_f32 v80, v82, v83
	v_cvt_pk_bf16_f32 v81, v84, v85
	v_pk_max_i16 v78, v78, 0
	v_pk_max_i16 v79, v79, 0
	v_pk_max_i16 v80, v80, 0
	v_pk_max_i16 v81, v81, 0
	s_waitcnt lgkmcnt(0)
	v_mfma_f32_32x32x16_bf16 v[50:65], v[66:69], v[86:89], v[50:65]
	v_mfma_f32_32x32x16_bf16 v[34:49], v[90:93], v[70:73], v[34:49]
	s_nop 10
	v_add_f32_e32 v130, v10, v58
	v_add_f32_e32 v131, v11, v59
	v_add_f32_e32 v132, v12, v60
	v_add_f32_e32 v133, v13, v61
	v_add_f32_e32 v138, v4, v52
	v_add_f32_e32 v139, v5, v53
	v_pk_add_f32 v[140:141], v[16:17], v[64:65]
	v_pk_add_f32 v[142:143], v[8:9], v[56:57]
	v_pk_add_f32 v[144:145], v[14:15], v[62:63]
	v_pk_add_f32 v[146:147], v[6:7], v[54:55]
	v_mfma_f32_32x32x16_bf16 v[18:33], v[102:105], v[70:73], v[18:33]
	ds_read2st64_b32 v[70:71], v135 offset0:133 offset1:134
	v_add_f32_e32 v148, v2, v50
	v_add_f32_e32 v149, v3, v51
	v_add_f32_e32 v144, v146, v144
	v_add_f32_e32 v145, v147, v145
	v_pk_add_f32 v[140:141], v[142:143], v[140:141]
	v_pk_add_f32 v[132:133], v[138:139], v[132:133]
	v_pk_add_f32 v[130:131], v[148:149], v[130:131]
	v_pk_add_f32 v[132:133], v[132:133], v[140:141]
	v_pk_add_f32 v[130:131], v[130:131], v[144:145]
	v_mfma_f32_32x32x16_bf16 v[34:49], v[66:69], v[78:81], v[34:49]
	s_waitcnt vmcnt(0) lgkmcnt(0)
	v_mul_f32_e32 v66, v175, v70
	v_add_f32_e32 v130, v131, v130
	v_add_f32_e32 v131, v132, v133
	ds_write_b32 v173, v66 offset:512
	v_mul_f32_e32 v66, v175, v71
	v_add_f32_e32 v130, v130, v131
	s_waitcnt lgkmcnt(0)
	ds_read_b128 v[102:105], v174 offset:34560
	ds_read_b128 v[98:101], v174 offset:34592
	ds_read_b128 v[110:113], v174 offset:34624
	ds_read_b128 v[106:109], v174 offset:34656
	ds_read_b128 v[114:117], v174 offset:34688
	ds_read_b128 v[122:125], v174 offset:34720
	ds_read_b128 v[118:121], v174 offset:34752
	ds_read_b128 v[126:129], v174 offset:34784
	v_mov_b32_dpp v66, v66 quad_perm:[1,0,3,2] row_mask:0xf bank_mask:0xf bound_ctrl:1
	v_mov_b32_e32 v131, v130
	v_fmac_f32_e32 v66, v175, v71
	s_nop 0
	v_permlane32_swap_b32_e32 v130, v131
	v_add_f32_dpp v66, v66, v66 quad_perm:[2,3,0,1] row_mask:0xf bank_mask:0xf bound_ctrl:1
	v_add_f32_e32 v130, v130, v131
	v_fmamk_f32 v65, v130, 0xbc800000, v65
	v_add_f32_dpp v66, v66, v66 row_half_mirror row_mask:0xf bank_mask:0xf bound_ctrl:1
	v_fmamk_f32 v64, v130, 0xbc800000, v64
	v_fmamk_f32 v63, v130, 0xbc800000, v63
	v_fmamk_f32 v62, v130, 0xbc800000, v62
	v_fmamk_f32 v61, v130, 0xbc800000, v61
	v_fmamk_f32 v60, v130, 0xbc800000, v60
	v_fmamk_f32 v59, v130, 0xbc800000, v59
	v_fmamk_f32 v58, v130, 0xbc800000, v58
	v_fmamk_f32 v57, v130, 0xbc800000, v57
	v_fmamk_f32 v56, v130, 0xbc800000, v56
	v_fmamk_f32 v55, v130, 0xbc800000, v55
	v_fmamk_f32 v54, v130, 0xbc800000, v54
	v_fmamk_f32 v53, v130, 0xbc800000, v53
	v_fmamk_f32 v52, v130, 0xbc800000, v52
	v_fmamk_f32 v51, v130, 0xbc800000, v51
	v_fmac_f32_e32 v50, 0xbc800000, v130
	v_add_f32_dpp v66, v66, v66 row_ror:8 row_mask:0xf bank_mask:0xf bound_ctrl:1
	v_fmamk_f32 v17, v130, 0xbc800000, v17
	v_fmamk_f32 v16, v130, 0xbc800000, v16
	v_fmamk_f32 v15, v130, 0xbc800000, v15
	v_fmamk_f32 v14, v130, 0xbc800000, v14
	v_fmamk_f32 v13, v130, 0xbc800000, v13
	v_fmamk_f32 v12, v130, 0xbc800000, v12
	v_fmamk_f32 v11, v130, 0xbc800000, v11
	v_fmamk_f32 v10, v130, 0xbc800000, v10
	v_fmamk_f32 v9, v130, 0xbc800000, v9
	v_fmamk_f32 v8, v130, 0xbc800000, v8
	v_fmamk_f32 v7, v130, 0xbc800000, v7
	v_fmamk_f32 v6, v130, 0xbc800000, v6
	v_fmamk_f32 v5, v130, 0xbc800000, v5
	v_fmamk_f32 v4, v130, 0xbc800000, v4
	v_fmamk_f32 v3, v130, 0xbc800000, v3
	v_fmac_f32_e32 v2, 0xbc800000, v130
	v_pk_mul_f32 v[130:131], v[54:55], v[54:55]
	v_pk_mul_f32 v[132:133], v[62:63], v[62:63]
	v_pk_mul_f32 v[138:139], v[50:51], v[50:51]
	v_pk_mul_f32 v[140:141], v[58:59], v[58:59]
	v_pk_mul_f32 v[142:143], v[56:57], v[56:57]
	v_pk_mul_f32 v[144:145], v[64:65], v[64:65]
	v_pk_mul_f32 v[146:147], v[52:53], v[52:53]
	v_pk_mul_f32 v[148:149], v[60:61], v[60:61]
	v_mov_b32_e32 v67, v66
	v_pk_fma_f32 v[148:149], v[12:13], v[12:13], v[148:149]
	v_pk_fma_f32 v[146:147], v[4:5], v[4:5], v[146:147]
	v_pk_fma_f32 v[144:145], v[16:17], v[16:17], v[144:145]
	v_pk_fma_f32 v[142:143], v[8:9], v[8:9], v[142:143]
	v_pk_fma_f32 v[140:141], v[10:11], v[10:11], v[140:141]
	v_pk_fma_f32 v[138:139], v[2:3], v[2:3], v[138:139]
	v_pk_fma_f32 v[132:133], v[14:15], v[14:15], v[132:133]
	v_pk_fma_f32 v[130:131], v[6:7], v[6:7], v[130:131]
	v_permlane16_swap_b32_e32 v66, v67
	v_pk_add_f32 v[130:131], v[130:131], v[132:133]
	v_pk_add_f32 v[132:133], v[138:139], v[140:141]
	v_pk_add_f32 v[138:139], v[142:143], v[144:145]
	v_pk_add_f32 v[140:141], v[146:147], v[148:149]
	v_mfma_f32_32x32x16_bf16 v[18:33], v[74:77], v[78:81], v[18:33]
	v_add_f32_e32 v136, v66, v67
	ds_read_b128 v[70:73], v134 offset:512
	ds_read_b128 v[66:69], v134 offset:544
	ds_read_b128 v[78:81], v134 offset:576
	ds_read_b128 v[74:77], v134 offset:608
	ds_read_b128 v[82:85], v134 offset:640
	ds_read_b128 v[90:93], v134 offset:672
	ds_read_b128 v[86:89], v134 offset:704
	ds_read_b128 v[94:97], v134 offset:736
	v_pk_add_f32 v[138:139], v[140:141], v[138:139]
	v_pk_add_f32 v[130:131], v[132:133], v[130:131]
	s_waitcnt lgkmcnt(8)
	v_pk_mul_f32 v[140:141], v[126:127], v[62:63]
	v_pk_mov_b32 v[132:133], v[130:131], v[138:139] op_sel:[1,0]
	v_mov_b32_e32 v131, v139
	v_pk_mul_f32 v[138:139], v[122:123], v[54:55]
	v_pk_mul_f32 v[142:143], v[114:115], v[50:51]
	v_pk_mul_f32 v[144:145], v[118:119], v[58:59]
	v_pk_mul_f32 v[146:147], v[124:125], v[56:57]
	v_pk_mul_f32 v[148:149], v[128:129], v[64:65]
	v_pk_mul_f32 v[154:155], v[116:117], v[52:53]
	v_pk_mul_f32 v[156:157], v[120:121], v[60:61]
	v_pk_fma_f32 v[154:155], v[104:105], v[4:5], v[154:155]
	v_pk_fma_f32 v[156:157], v[112:113], v[12:13], v[156:157]
	v_pk_fma_f32 v[148:149], v[108:109], v[16:17], v[148:149]
	v_pk_fma_f32 v[146:147], v[100:101], v[8:9], v[146:147]
	v_pk_fma_f32 v[144:145], v[110:111], v[10:11], v[144:145]
	v_pk_fma_f32 v[142:143], v[102:103], v[2:3], v[142:143]
	v_pk_fma_f32 v[140:141], v[106:107], v[14:15], v[140:141]
	v_pk_fma_f32 v[138:139], v[98:99], v[6:7], v[138:139]
	v_pk_add_f32 v[130:131], v[132:133], v[130:131]
	v_pk_add_f32 v[138:139], v[138:139], v[140:141]
	v_pk_add_f32 v[140:141], v[142:143], v[144:145]
	v_pk_add_f32 v[142:143], v[146:147], v[148:149]
	v_pk_add_f32 v[144:145], v[154:155], v[156:157]
	v_pk_add_f32 v[132:133], v[130:131], v[130:131] op_sel:[0,1] op_sel_hi:[1,0]
	v_pk_add_f32 v[142:143], v[144:145], v[142:143]
	v_pk_add_f32 v[138:139], v[140:141], v[138:139]
	v_add_f32_e32 v133, v142, v143
	v_add_f32_e32 v130, v138, v139
	s_waitcnt lgkmcnt(2)
	v_pk_mul_f32 v[138:139], v[90:91], v[54:55]
	s_waitcnt lgkmcnt(0)
	v_pk_mul_f32 v[140:141], v[94:95], v[62:63]
	v_pk_mul_f32 v[142:143], v[82:83], v[50:51]
	v_pk_mul_f32 v[144:145], v[86:87], v[58:59]
	v_pk_mul_f32 v[146:147], v[92:93], v[56:57]
	v_pk_mul_f32 v[148:149], v[96:97], v[64:65]
	v_pk_mul_f32 v[154:155], v[84:85], v[52:53]
	v_pk_mul_f32 v[156:157], v[88:89], v[60:61]
	v_add_f32_e32 v130, v130, v133
	v_pk_fma_f32 v[156:157], v[80:81], v[12:13], v[156:157]
	v_pk_fma_f32 v[154:155], v[72:73], v[4:5], v[154:155]
	v_pk_fma_f32 v[148:149], v[76:77], v[16:17], v[148:149]
	v_pk_fma_f32 v[146:147], v[68:69], v[8:9], v[146:147]
	v_pk_fma_f32 v[144:145], v[78:79], v[10:11], v[144:145]
	v_pk_fma_f32 v[142:143], v[70:71], v[2:3], v[142:143]
	v_pk_fma_f32 v[140:141], v[74:75], v[14:15], v[140:141]
	v_pk_fma_f32 v[138:139], v[66:67], v[6:7], v[138:139]
	v_mov_b32_e32 v133, v130
	v_pk_add_f32 v[138:139], v[138:139], v[140:141]
	v_pk_add_f32 v[140:141], v[142:143], v[144:145]
	v_pk_add_f32 v[142:143], v[146:147], v[148:149]
	v_pk_add_f32 v[144:145], v[154:155], v[156:157]
	v_permlane32_swap_b32_e32 v130, v133
	v_pk_add_f32 v[142:143], v[144:145], v[142:143]
	v_add_f32_e32 v160, v130, v133
	v_pk_add_f32 v[138:139], v[140:141], v[138:139]
	v_add_f32_e32 v133, v142, v143
	v_pk_add_f32 v[140:141], v[26:27], v[42:43]
	v_pk_add_f32 v[142:143], v[28:29], v[44:45]
	v_pk_add_f32 v[144:145], v[20:21], v[36:37]
	v_pk_add_f32 v[146:147], v[32:33], v[48:49]
	v_pk_add_f32 v[148:149], v[24:25], v[40:41]
	v_pk_add_f32 v[154:155], v[30:31], v[46:47]
	v_pk_add_f32 v[156:157], v[22:23], v[38:39]
	v_pk_add_f32 v[158:159], v[18:19], v[34:35]
	v_pk_add_f32 v[154:155], v[156:157], v[154:155]
	v_pk_add_f32 v[146:147], v[148:149], v[146:147]
	v_pk_add_f32 v[142:143], v[144:145], v[142:143]
	v_pk_add_f32 v[140:141], v[158:159], v[140:141]
	v_pk_add_f32 v[142:143], v[142:143], v[146:147]
	v_pk_add_f32 v[140:141], v[140:141], v[154:155]
	v_add_f32_e32 v130, v138, v139
	v_add_f32_e32 v140, v141, v140
	v_add_f32_e32 v141, v142, v143
	v_add_f32_e32 v133, v130, v133
	v_add_f32_e32 v140, v140, v141
	v_mov_b32_e32 v131, v132
	v_mov_b32_e32 v130, v140
	s_nop 1
	v_permlane32_swap_b32_e32 v140, v130
	v_add_f32_e32 v130, v140, v130
	v_fmamk_f32 v49, v130, 0xbc800000, v49
	v_fmamk_f32 v48, v130, 0xbc800000, v48
	v_fmamk_f32 v47, v130, 0xbc800000, v47
	v_fmamk_f32 v46, v130, 0xbc800000, v46
	v_fmamk_f32 v45, v130, 0xbc800000, v45
	v_fmamk_f32 v44, v130, 0xbc800000, v44
	v_fmamk_f32 v43, v130, 0xbc800000, v43
	v_fmamk_f32 v42, v130, 0xbc800000, v42
	v_fmamk_f32 v41, v130, 0xbc800000, v41
	v_fmamk_f32 v40, v130, 0xbc800000, v40
	v_fmamk_f32 v39, v130, 0xbc800000, v39
	v_fmamk_f32 v38, v130, 0xbc800000, v38
	v_fmamk_f32 v37, v130, 0xbc800000, v37
	v_fmamk_f32 v36, v130, 0xbc800000, v36
	v_fmamk_f32 v35, v130, 0xbc800000, v35
	v_fmac_f32_e32 v34, 0xbc800000, v130
	v_fmamk_f32 v33, v130, 0xbc800000, v33
	v_fmamk_f32 v32, v130, 0xbc800000, v32
	v_fmamk_f32 v31, v130, 0xbc800000, v31
	v_fmamk_f32 v30, v130, 0xbc800000, v30
	v_fmamk_f32 v29, v130, 0xbc800000, v29
	v_fmamk_f32 v28, v130, 0xbc800000, v28
	v_fmamk_f32 v27, v130, 0xbc800000, v27
	v_fmamk_f32 v26, v130, 0xbc800000, v26
	v_fmamk_f32 v25, v130, 0xbc800000, v25
	v_fmamk_f32 v24, v130, 0xbc800000, v24
	v_fmamk_f32 v23, v130, 0xbc800000, v23
	v_fmamk_f32 v22, v130, 0xbc800000, v22
	v_fmamk_f32 v21, v130, 0xbc800000, v21
	v_fmamk_f32 v20, v130, 0xbc800000, v20
	v_fmamk_f32 v19, v130, 0xbc800000, v19
	v_fmac_f32_e32 v18, 0xbc800000, v130
	v_pk_mul_f32 v[140:141], v[38:39], v[38:39]
	v_pk_mul_f32 v[142:143], v[46:47], v[46:47]
	v_pk_mul_f32 v[144:145], v[34:35], v[34:35]
	v_pk_mul_f32 v[146:147], v[42:43], v[42:43]
	v_pk_mul_f32 v[148:149], v[40:41], v[40:41]
	v_pk_mul_f32 v[154:155], v[48:49], v[48:49]
	v_pk_mul_f32 v[156:157], v[36:37], v[36:37]
	v_pk_mul_f32 v[158:159], v[44:45], v[44:45]
	v_pk_fma_f32 v[156:157], v[20:21], v[20:21], v[156:157]
	v_pk_fma_f32 v[158:159], v[28:29], v[28:29], v[158:159]
	v_pk_fma_f32 v[154:155], v[32:33], v[32:33], v[154:155]
	v_pk_fma_f32 v[148:149], v[24:25], v[24:25], v[148:149]
	v_pk_fma_f32 v[146:147], v[26:27], v[26:27], v[146:147]
	v_pk_fma_f32 v[144:145], v[18:19], v[18:19], v[144:145]
	v_pk_fma_f32 v[142:143], v[30:31], v[30:31], v[142:143]
	v_pk_fma_f32 v[140:141], v[22:23], v[22:23], v[140:141]
	v_permlane32_swap_b32_e32 v132, v131
	v_pk_add_f32 v[140:141], v[140:141], v[142:143]
	v_pk_add_f32 v[142:143], v[144:145], v[146:147]
	v_pk_add_f32 v[144:145], v[148:149], v[154:155]
	v_pk_add_f32 v[146:147], v[156:157], v[158:159]
	v_pk_add_f32 v[140:141], v[142:143], v[140:141]
	v_pk_add_f32 v[144:145], v[146:147], v[144:145]
	v_pk_mul_f32 v[122:123], v[122:123], v[38:39]
	v_pk_mov_b32 v[142:143], v[140:141], v[144:145] op_sel:[1,0]
	v_mov_b32_e32 v141, v145
	v_pk_add_f32 v[140:141], v[142:143], v[140:141]
	v_pk_mul_f32 v[126:127], v[126:127], v[46:47]
	v_pk_add_f32 v[140:141], v[140:141], v[140:141] op_sel:[0,1] op_sel_hi:[1,0]
	v_pk_mul_f32 v[114:115], v[114:115], v[34:35]
	v_mov_b32_e32 v130, v140
	s_nop 1
	v_permlane32_swap_b32_e32 v140, v130
	v_mov_b32_e32 v141, v132
	v_pk_add_f32 v[130:131], v[140:141], v[130:131]
	v_pk_mul_f32 v[118:119], v[118:119], v[42:43]
	v_pk_fma_f32 v[130:131], v[130:131], s[0:1], v[152:153] op_sel_hi:[1,0,0]
	v_pk_mul_f32 v[124:125], v[124:125], v[40:41]
	v_pk_mul_f32 v[128:129], v[128:129], v[48:49]
	v_pk_mul_f32 v[116:117], v[116:117], v[36:37]
	v_pk_mul_f32 v[120:121], v[120:121], v[44:45]
	v_pk_fma_f32 v[112:113], v[112:113], v[28:29], v[120:121]
	v_pk_fma_f32 v[104:105], v[104:105], v[20:21], v[116:117]
	v_pk_fma_f32 v[108:109], v[108:109], v[32:33], v[128:129]
	v_pk_fma_f32 v[100:101], v[100:101], v[24:25], v[124:125]
	v_pk_fma_f32 v[110:111], v[110:111], v[26:27], v[118:119]
	v_pk_fma_f32 v[102:103], v[102:103], v[18:19], v[114:115]
	v_pk_fma_f32 v[106:107], v[106:107], v[30:31], v[126:127]
	v_pk_fma_f32 v[98:99], v[98:99], v[22:23], v[122:123]
	v_rsq_f32_e32 v131, v131
	v_pk_add_f32 v[98:99], v[98:99], v[106:107]
	v_pk_add_f32 v[102:103], v[102:103], v[110:111]
	v_pk_add_f32 v[100:101], v[100:101], v[108:109]
	v_pk_add_f32 v[104:105], v[104:105], v[112:113]
	v_rsq_f32_e32 v132, v130
	v_pk_add_f32 v[100:101], v[104:105], v[100:101]
	v_pk_add_f32 v[98:99], v[102:103], v[98:99]
	v_add_f32_e32 v98, v98, v99
	v_add_f32_e32 v99, v100, v101
	v_add_f32_e32 v98, v98, v99
	v_mov_b32_e32 v99, v98
	v_pk_mul_f32 v[90:91], v[90:91], v[38:39]
	v_pk_mul_f32 v[94:95], v[94:95], v[46:47]
	v_pk_mul_f32 v[82:83], v[82:83], v[34:35]
	v_pk_mul_f32 v[86:87], v[86:87], v[42:43]
	v_permlane32_swap_b32_e32 v98, v99
	v_pk_fma_f32 v[78:79], v[78:79], v[26:27], v[86:87]
	v_pk_fma_f32 v[70:71], v[70:71], v[18:19], v[82:83]
	v_pk_fma_f32 v[74:75], v[74:75], v[30:31], v[94:95]
	v_pk_fma_f32 v[66:67], v[66:67], v[22:23], v[90:91]
	v_mov_b32_e32 v130, v131
	v_mov_b32_e32 v131, v132
	v_add_f32_e32 v98, v98, v99
	v_pk_add_f32 v[66:67], v[66:67], v[74:75]
	v_pk_add_f32 v[70:71], v[70:71], v[78:79]
	v_mul_f32_e32 v139, v160, v130
	v_mul_f32_e32 v98, v98, v131
	v_pk_add_f32 v[66:67], v[70:71], v[66:67]
	v_cmp_gt_u32_e32 vcc, 32, v1
	v_add_f32_e32 v66, v66, v67
	v_pk_mul_f32 v[92:93], v[92:93], v[40:41]
	v_cndmask_b32_e32 v67, v98, v139, vcc
	v_add_f32_e32 v67, s12, v67
	v_pk_mul_f32 v[96:97], v[96:97], v[48:49]
	v_pk_mul_f32 v[84:85], v[84:85], v[36:37]
	v_pk_mul_f32 v[88:89], v[88:89], v[44:45]
	v_mul_f32_e32 v67, 0xbfb8aa3b, v67
	v_pk_fma_f32 v[80:81], v[80:81], v[28:29], v[88:89]
	v_pk_fma_f32 v[72:73], v[72:73], v[20:21], v[84:85]
	v_pk_fma_f32 v[76:77], v[76:77], v[32:33], v[96:97]
	v_pk_fma_f32 v[68:69], v[68:69], v[24:25], v[92:93]
	v_exp_f32_e32 v70, v67
	v_pk_add_f32 v[68:69], v[68:69], v[76:77]
	v_pk_add_f32 v[72:73], v[72:73], v[80:81]
	v_cmp_lt_i32_e64 s[0:1], 0, v151
	v_pk_add_f32 v[68:69], v[72:73], v[68:69]
	v_mov_b32_e32 v137, v136
	v_add_f32_e32 v67, v68, v69
	v_add_f32_e32 v67, v66, v67
	v_add_f32_e32 v66, 1.0, v70
	v_rcp_f32_e32 v66, v66
	v_mov_b32_e32 v69, 0xff800000
	v_mov_b32_e32 v138, v133
	v_mov_b32_e32 v68, v67
	v_cndmask_b32_e64 v70, v69, v66, s[0:1]
	v_mbcnt_lo_u32_b32 v66, -1, 0
	v_mbcnt_hi_u32_b32 v66, -1, v66
	v_permlane32_swap_b32_e32 v136, v137
	v_permlane32_swap_b32_e32 v133, v138
	v_permlane32_swap_b32_e32 v67, v68
	v_and_b32_e32 v86, 64, v66
	s_mov_b32 s14, 8
	s_mov_b32 s13, 0
	v_mov_b32_e32 v66, 0
	s_waitcnt lgkmcnt(0)
